# nt cache hint on the attention output (O) stores, read once by phase 4; on top of v48 (ys-store hint of v49 dropped)
# speedup vs baseline: 1.0096x; 1.0096x over previous
; __device__ __forceinline__ int crow(int r, int hi) { return (r & 3) + 8 * (r >> 2) + 4 * hi; }
; __device__ __forceinline__ void block(const Blk& B, char* lds, A3_LAS unsigned char* ldsl, const int tid) {
;     ...
;     { auto rr = __builtin_amdgcn_permlane32_swap(__float_as_uint(l_reg), __float_as_uint(l_reg), false, false); l_reg = __uint_as_float(rr[0]) + __uint_as_float(rr[1]); }
;     if (hi == 0) sc_l[32 + r32] = l_reg;
;     asm volatile("s_waitcnt lgkmcnt(0)" ::: "memory");
;     float rli[16];
; #pragma unroll
;     for (int r = 0; r < 16; ++r) rli[r] = __builtin_amdgcn_rcpf(sc_l[32 + attn::crow(r, hi)]);
;     abf* Ow = B.O + (size_t)(wid * 32) * LDO;
; #pragma unroll
;     for (int r = 0; r < 16; ++r) { const int orow = attn::crow(r, hi);
; #pragma unroll
;         for (int d0 = 0; d0 < 8; ++d0) { const float v = o[d0][r] * rli[r]; const float vn = __shfl_xor(v, 1);
;             if ((r32 & 1) == 0) *(unsigned*)(Ow + (size_t)orow * LDO + d0 * 32 + r32) = attn::cvtpk(v, vn); } }
.LBB0_338:
	v_mov_b32_e32 v0, v146
	s_nop 1
	v_permlane32_swap_b32_e32 v146, v0
	s_and_saveexec_b64 s[58:59], s[2:3]
	v_add_f32_e32 v0, v146, v0
	ds_write_b32 v204, v0 offset:128
	s_or_b64 exec, exec, s[58:59]
	s_waitcnt lgkmcnt(0)
	ds_read_b128 v[142:145], v203 offset:128
	ds_read_b128 v[138:141], v203 offset:160
	ds_read_b128 v[134:137], v203 offset:192
	ds_read_b128 v[130:133], v203 offset:224
	s_lshl_b32 s2, s6, 21
	s_add_u32 s4, s67, s2
	s_addc_u32 s5, s24, 0
	s_ashr_i32 s57, s56, 31
	s_lshl_b64 s[2:3], s[56:57], 13
	s_add_u32 s4, s4, s2
	s_addc_u32 s5, s5, s3
	v_lshlrev_b32_e32 v0, 1, v196
	v_lshl_add_u64 v[146:147], s[4:5], 0, v[0:1]
	v_lshlrev_b32_e32 v0, 15, v198
	v_lshl_add_u64 v[146:147], v[146:147], 0, v[0:1]
	v_and_b32_e32 v0, 1, v197
	v_cmp_eq_u32_e64 s[2:3], 0, v0
	s_waitcnt lgkmcnt(0)
	v_rcp_f32_e32 v142, v142
	v_rcp_f32_e32 v143, v143
	v_rcp_f32_e32 v144, v144
	v_rcp_f32_e32 v145, v145
	v_rcp_f32_e32 v138, v138
	v_rcp_f32_e32 v139, v139
	v_rcp_f32_e32 v140, v140
	v_rcp_f32_e32 v141, v141
	v_rcp_f32_e32 v134, v134
	v_rcp_f32_e32 v135, v135
	v_rcp_f32_e32 v136, v136
	v_rcp_f32_e32 v137, v137
	v_rcp_f32_e32 v130, v130
	v_rcp_f32_e32 v131, v131
	v_rcp_f32_e32 v132, v132
	v_rcp_f32_e32 v133, v133
	s_nop 0
	v_mul_f32_e32 v212, v114, v142
	v_mul_f32_e32 v213, v98, v142
	v_mul_f32_e32 v214, v82, v142
	v_mul_f32_e32 v215, v66, v142
	v_mul_f32_e32 v216, v50, v142
	v_mul_f32_e32 v217, v34, v142
	v_mul_f32_e32 v218, v18, v142
	v_mul_f32_e32 v219, v2, v142
	v_mov_b32_dpp v220, v212 quad_perm:[1,0,3,2] row_mask:0xf bank_mask:0xf
	v_mov_b32_dpp v221, v213 quad_perm:[1,0,3,2] row_mask:0xf bank_mask:0xf
	v_mov_b32_dpp v222, v214 quad_perm:[1,0,3,2] row_mask:0xf bank_mask:0xf
	v_mov_b32_dpp v223, v215 quad_perm:[1,0,3,2] row_mask:0xf bank_mask:0xf
	v_mov_b32_dpp v224, v216 quad_perm:[1,0,3,2] row_mask:0xf bank_mask:0xf
	v_mov_b32_dpp v225, v217 quad_perm:[1,0,3,2] row_mask:0xf bank_mask:0xf
	v_mov_b32_dpp v226, v218 quad_perm:[1,0,3,2] row_mask:0xf bank_mask:0xf
	v_mov_b32_dpp v227, v219 quad_perm:[1,0,3,2] row_mask:0xf bank_mask:0xf
	v_cvt_pk_bf16_f32 v212, v212, v220
	v_cvt_pk_bf16_f32 v213, v213, v221
	v_cvt_pk_bf16_f32 v214, v214, v222
	v_cvt_pk_bf16_f32 v215, v215, v223
	v_cvt_pk_bf16_f32 v216, v216, v224
	v_cvt_pk_bf16_f32 v217, v217, v225
	v_cvt_pk_bf16_f32 v218, v218, v226
	v_cvt_pk_bf16_f32 v219, v219, v227
	s_mov_b64 exec, s[2:3]
	global_store_dword v[146:147], v212, off nt
	global_store_dword v[146:147], v213, off offset:64 nt
	global_store_dword v[146:147], v214, off offset:128 nt
	global_store_dword v[146:147], v215, off offset:192 nt
	global_store_dword v[146:147], v216, off offset:256 nt
	global_store_dword v[146:147], v217, off offset:320 nt
	global_store_dword v[146:147], v218, off offset:384 nt
	global_store_dword v[146:147], v219, off offset:448 nt
	s_mov_b64 exec, -1
	s_mov_b64 s[60:61], 0x2000
	v_lshl_add_u64 v[228:229], v[146:147], 0, s[60:61]
	v_mul_f32_e32 v230, v115, v143
	v_mul_f32_e32 v231, v99, v143
	v_mul_f32_e32 v232, v83, v143
	v_mul_f32_e32 v233, v67, v143
	v_mul_f32_e32 v234, v51, v143
	v_mul_f32_e32 v235, v35, v143
	v_mul_f32_e32 v236, v19, v143
	v_mul_f32_e32 v237, v3, v143
	v_mov_b32_dpp v238, v230 quad_perm:[1,0,3,2] row_mask:0xf bank_mask:0xf
	v_mov_b32_dpp v239, v231 quad_perm:[1,0,3,2] row_mask:0xf bank_mask:0xf
	v_mov_b32_dpp v240, v232 quad_perm:[1,0,3,2] row_mask:0xf bank_mask:0xf
	v_mov_b32_dpp v241, v233 quad_perm:[1,0,3,2] row_mask:0xf bank_mask:0xf
	v_mov_b32_dpp v242, v234 quad_perm:[1,0,3,2] row_mask:0xf bank_mask:0xf
	v_mov_b32_dpp v243, v235 quad_perm:[1,0,3,2] row_mask:0xf bank_mask:0xf
	v_mov_b32_dpp v244, v236 quad_perm:[1,0,3,2] row_mask:0xf bank_mask:0xf
	v_mov_b32_dpp v245, v237 quad_perm:[1,0,3,2] row_mask:0xf bank_mask:0xf
	v_cvt_pk_bf16_f32 v230, v230, v238
	v_cvt_pk_bf16_f32 v231, v231, v239
	v_cvt_pk_bf16_f32 v232, v232, v240
	v_cvt_pk_bf16_f32 v233, v233, v241
	v_cvt_pk_bf16_f32 v234, v234, v242
	v_cvt_pk_bf16_f32 v235, v235, v243
	v_cvt_pk_bf16_f32 v236, v236, v244
	v_cvt_pk_bf16_f32 v237, v237, v245
	s_mov_b64 exec, s[2:3]
	global_store_dword v[228:229], v230, off nt
	global_store_dword v[228:229], v231, off offset:64 nt
	global_store_dword v[228:229], v232, off offset:128 nt
	global_store_dword v[228:229], v233, off offset:192 nt
	global_store_dword v[228:229], v234, off offset:256 nt
	global_store_dword v[228:229], v235, off offset:320 nt
	global_store_dword v[228:229], v236, off offset:384 nt
	global_store_dword v[228:229], v237, off offset:448 nt
	s_mov_b64 exec, -1
	s_mov_b64 s[60:61], 0x4000
	v_lshl_add_u64 v[228:229], v[146:147], 0, s[60:61]
	v_mul_f32_e32 v212, v116, v144
	v_mul_f32_e32 v213, v100, v144
	v_mul_f32_e32 v214, v84, v144
	v_mul_f32_e32 v215, v68, v144
	v_mul_f32_e32 v216, v52, v144
	v_mul_f32_e32 v217, v36, v144
	v_mul_f32_e32 v218, v20, v144
	v_mul_f32_e32 v219, v4, v144
	v_mov_b32_dpp v220, v212 quad_perm:[1,0,3,2] row_mask:0xf bank_mask:0xf
	v_mov_b32_dpp v221, v213 quad_perm:[1,0,3,2] row_mask:0xf bank_mask:0xf
	v_mov_b32_dpp v222, v214 quad_perm:[1,0,3,2] row_mask:0xf bank_mask:0xf
	v_mov_b32_dpp v223, v215 quad_perm:[1,0,3,2] row_mask:0xf bank_mask:0xf
	v_mov_b32_dpp v224, v216 quad_perm:[1,0,3,2] row_mask:0xf bank_mask:0xf
	v_mov_b32_dpp v225, v217 quad_perm:[1,0,3,2] row_mask:0xf bank_mask:0xf
	v_mov_b32_dpp v226, v218 quad_perm:[1,0,3,2] row_mask:0xf bank_mask:0xf
	v_mov_b32_dpp v227, v219 quad_perm:[1,0,3,2] row_mask:0xf bank_mask:0xf
	v_cvt_pk_bf16_f32 v212, v212, v220
	v_cvt_pk_bf16_f32 v213, v213, v221
	v_cvt_pk_bf16_f32 v214, v214, v222
	v_cvt_pk_bf16_f32 v215, v215, v223
	v_cvt_pk_bf16_f32 v216, v216, v224
	v_cvt_pk_bf16_f32 v217, v217, v225
; __device__ __forceinline__ int crow(int r, int hi) { return (r & 3) + 8 * (r >> 2) + 4 * hi; }
; __device__ __forceinline__ void block(const Blk& B, char* lds, A3_LAS unsigned char* ldsl, const int tid) {
;     ...
;     for (int r = 0; r < 16; ++r) { const int orow = attn::crow(r, hi);
; #pragma unroll
;         for (int d0 = 0; d0 < 8; ++d0) { const float v = o[d0][r] * rli[r]; const float vn = __shfl_xor(v, 1);
;             if ((r32 & 1) == 0) *(unsigned*)(Ow + (size_t)orow * LDO + d0 * 32 + r32) = attn::cvtpk(v, vn); } }
	v_cvt_pk_bf16_f32 v218, v218, v226
	v_cvt_pk_bf16_f32 v219, v219, v227
	s_mov_b64 exec, s[2:3]
	global_store_dword v[228:229], v212, off nt
	global_store_dword v[228:229], v213, off offset:64 nt
	global_store_dword v[228:229], v214, off offset:128 nt
	global_store_dword v[228:229], v215, off offset:192 nt
	global_store_dword v[228:229], v216, off offset:256 nt
	global_store_dword v[228:229], v217, off offset:320 nt
	global_store_dword v[228:229], v218, off offset:384 nt
	global_store_dword v[228:229], v219, off offset:448 nt
	s_mov_b64 exec, -1
	s_mov_b64 s[60:61], 0x6000
	v_lshl_add_u64 v[228:229], v[146:147], 0, s[60:61]
	v_mul_f32_e32 v230, v117, v145
	v_mul_f32_e32 v231, v101, v145
	v_mul_f32_e32 v232, v85, v145
	v_mul_f32_e32 v233, v69, v145
	v_mul_f32_e32 v234, v53, v145
	v_mul_f32_e32 v235, v37, v145
	v_mul_f32_e32 v236, v21, v145
	v_mul_f32_e32 v237, v5, v145
	v_mov_b32_dpp v238, v230 quad_perm:[1,0,3,2] row_mask:0xf bank_mask:0xf
	v_mov_b32_dpp v239, v231 quad_perm:[1,0,3,2] row_mask:0xf bank_mask:0xf
	v_mov_b32_dpp v240, v232 quad_perm:[1,0,3,2] row_mask:0xf bank_mask:0xf
	v_mov_b32_dpp v241, v233 quad_perm:[1,0,3,2] row_mask:0xf bank_mask:0xf
	v_mov_b32_dpp v242, v234 quad_perm:[1,0,3,2] row_mask:0xf bank_mask:0xf
	v_mov_b32_dpp v243, v235 quad_perm:[1,0,3,2] row_mask:0xf bank_mask:0xf
	v_mov_b32_dpp v244, v236 quad_perm:[1,0,3,2] row_mask:0xf bank_mask:0xf
	v_mov_b32_dpp v245, v237 quad_perm:[1,0,3,2] row_mask:0xf bank_mask:0xf
	v_cvt_pk_bf16_f32 v230, v230, v238
	v_cvt_pk_bf16_f32 v231, v231, v239
	v_cvt_pk_bf16_f32 v232, v232, v240
	v_cvt_pk_bf16_f32 v233, v233, v241
	v_cvt_pk_bf16_f32 v234, v234, v242
	v_cvt_pk_bf16_f32 v235, v235, v243
	v_cvt_pk_bf16_f32 v236, v236, v244
	v_cvt_pk_bf16_f32 v237, v237, v245
	s_mov_b64 exec, s[2:3]
	global_store_dword v[228:229], v230, off nt
	global_store_dword v[228:229], v231, off offset:64 nt
	global_store_dword v[228:229], v232, off offset:128 nt
	global_store_dword v[228:229], v233, off offset:192 nt
	global_store_dword v[228:229], v234, off offset:256 nt
	global_store_dword v[228:229], v235, off offset:320 nt
	global_store_dword v[228:229], v236, off offset:384 nt
	global_store_dword v[228:229], v237, off offset:448 nt
	s_mov_b64 exec, -1
	s_mov_b64 s[60:61], 0x10000
	v_lshl_add_u64 v[228:229], v[146:147], 0, s[60:61]
	v_mul_f32_e32 v212, v118, v138
	v_mul_f32_e32 v213, v102, v138
	v_mul_f32_e32 v214, v86, v138
	v_mul_f32_e32 v215, v70, v138
	v_mul_f32_e32 v216, v54, v138
	v_mul_f32_e32 v217, v38, v138
	v_mul_f32_e32 v218, v22, v138
	v_mul_f32_e32 v219, v6, v138
	v_mov_b32_dpp v220, v212 quad_perm:[1,0,3,2] row_mask:0xf bank_mask:0xf
	v_mov_b32_dpp v221, v213 quad_perm:[1,0,3,2] row_mask:0xf bank_mask:0xf
	v_mov_b32_dpp v222, v214 quad_perm:[1,0,3,2] row_mask:0xf bank_mask:0xf
	v_mov_b32_dpp v223, v215 quad_perm:[1,0,3,2] row_mask:0xf bank_mask:0xf
	v_mov_b32_dpp v224, v216 quad_perm:[1,0,3,2] row_mask:0xf bank_mask:0xf
	v_mov_b32_dpp v225, v217 quad_perm:[1,0,3,2] row_mask:0xf bank_mask:0xf
	v_mov_b32_dpp v226, v218 quad_perm:[1,0,3,2] row_mask:0xf bank_mask:0xf
	v_mov_b32_dpp v227, v219 quad_perm:[1,0,3,2] row_mask:0xf bank_mask:0xf
	v_cvt_pk_bf16_f32 v212, v212, v220
	v_cvt_pk_bf16_f32 v213, v213, v221
	v_cvt_pk_bf16_f32 v214, v214, v222
	v_cvt_pk_bf16_f32 v215, v215, v223
	v_cvt_pk_bf16_f32 v216, v216, v224
	v_cvt_pk_bf16_f32 v217, v217, v225
	v_cvt_pk_bf16_f32 v218, v218, v226
	v_cvt_pk_bf16_f32 v219, v219, v227
	s_mov_b64 exec, s[2:3]
	global_store_dword v[228:229], v212, off nt
	global_store_dword v[228:229], v213, off offset:64 nt
	global_store_dword v[228:229], v214, off offset:128 nt
	global_store_dword v[228:229], v215, off offset:192 nt
	global_store_dword v[228:229], v216, off offset:256 nt
	global_store_dword v[228:229], v217, off offset:320 nt
	global_store_dword v[228:229], v218, off offset:384 nt
	global_store_dword v[228:229], v219, off offset:448 nt
	s_mov_b64 exec, -1
	s_mov_b64 s[60:61], 0x12000
	v_lshl_add_u64 v[228:229], v[146:147], 0, s[60:61]
	v_mul_f32_e32 v230, v119, v139
	v_mul_f32_e32 v231, v103, v139
	v_mul_f32_e32 v232, v87, v139
	v_mul_f32_e32 v233, v71, v139
	v_mul_f32_e32 v234, v55, v139
	v_mul_f32_e32 v235, v39, v139
	v_mul_f32_e32 v236, v23, v139
	v_mul_f32_e32 v237, v7, v139
	v_mov_b32_dpp v238, v230 quad_perm:[1,0,3,2] row_mask:0xf bank_mask:0xf
	v_mov_b32_dpp v239, v231 quad_perm:[1,0,3,2] row_mask:0xf bank_mask:0xf
	v_mov_b32_dpp v240, v232 quad_perm:[1,0,3,2] row_mask:0xf bank_mask:0xf
	v_mov_b32_dpp v241, v233 quad_perm:[1,0,3,2] row_mask:0xf bank_mask:0xf
	v_mov_b32_dpp v242, v234 quad_perm:[1,0,3,2] row_mask:0xf bank_mask:0xf
	v_mov_b32_dpp v243, v235 quad_perm:[1,0,3,2] row_mask:0xf bank_mask:0xf
	v_mov_b32_dpp v244, v236 quad_perm:[1,0,3,2] row_mask:0xf bank_mask:0xf
	v_mov_b32_dpp v245, v237 quad_perm:[1,0,3,2] row_mask:0xf bank_mask:0xf
	v_cvt_pk_bf16_f32 v230, v230, v238
	v_cvt_pk_bf16_f32 v231, v231, v239
	v_cvt_pk_bf16_f32 v232, v232, v240
	v_cvt_pk_bf16_f32 v233, v233, v241
	v_cvt_pk_bf16_f32 v234, v234, v242
	v_cvt_pk_bf16_f32 v235, v235, v243
	v_cvt_pk_bf16_f32 v236, v236, v244
	v_cvt_pk_bf16_f32 v237, v237, v245
	s_mov_b64 exec, s[2:3]
	global_store_dword v[228:229], v230, off nt
	global_store_dword v[228:229], v231, off offset:64 nt
	global_store_dword v[228:229], v232, off offset:128 nt
	global_store_dword v[228:229], v233, off offset:192 nt
	global_store_dword v[228:229], v234, off offset:256 nt
	global_store_dword v[228:229], v235, off offset:320 nt
	global_store_dword v[228:229], v236, off offset:384 nt
	global_store_dword v[228:229], v237, off offset:448 nt
	s_mov_b64 exec, -1
	s_mov_b64 s[60:61], 0x14000
; __device__ __forceinline__ int crow(int r, int hi) { return (r & 3) + 8 * (r >> 2) + 4 * hi; }
; __device__ __forceinline__ void block(const Blk& B, char* lds, A3_LAS unsigned char* ldsl, const int tid) {
;     ...
;     for (int r = 0; r < 16; ++r) { const int orow = attn::crow(r, hi);
; #pragma unroll
;         for (int d0 = 0; d0 < 8; ++d0) { const float v = o[d0][r] * rli[r]; const float vn = __shfl_xor(v, 1);
;             if ((r32 & 1) == 0) *(unsigned*)(Ow + (size_t)orow * LDO + d0 * 32 + r32) = attn::cvtpk(v, vn); } }
	v_lshl_add_u64 v[228:229], v[146:147], 0, s[60:61]
	v_mul_f32_e32 v212, v120, v140
	v_mul_f32_e32 v213, v104, v140
	v_mul_f32_e32 v214, v88, v140
	v_mul_f32_e32 v215, v72, v140
	v_mul_f32_e32 v216, v56, v140
	v_mul_f32_e32 v217, v40, v140
	v_mul_f32_e32 v218, v24, v140
	v_mul_f32_e32 v219, v8, v140
	v_mov_b32_dpp v220, v212 quad_perm:[1,0,3,2] row_mask:0xf bank_mask:0xf
	v_mov_b32_dpp v221, v213 quad_perm:[1,0,3,2] row_mask:0xf bank_mask:0xf
	v_mov_b32_dpp v222, v214 quad_perm:[1,0,3,2] row_mask:0xf bank_mask:0xf
	v_mov_b32_dpp v223, v215 quad_perm:[1,0,3,2] row_mask:0xf bank_mask:0xf
	v_mov_b32_dpp v224, v216 quad_perm:[1,0,3,2] row_mask:0xf bank_mask:0xf
	v_mov_b32_dpp v225, v217 quad_perm:[1,0,3,2] row_mask:0xf bank_mask:0xf
	v_mov_b32_dpp v226, v218 quad_perm:[1,0,3,2] row_mask:0xf bank_mask:0xf
	v_mov_b32_dpp v227, v219 quad_perm:[1,0,3,2] row_mask:0xf bank_mask:0xf
	v_cvt_pk_bf16_f32 v212, v212, v220
	v_cvt_pk_bf16_f32 v213, v213, v221
	v_cvt_pk_bf16_f32 v214, v214, v222
	v_cvt_pk_bf16_f32 v215, v215, v223
	v_cvt_pk_bf16_f32 v216, v216, v224
	v_cvt_pk_bf16_f32 v217, v217, v225
	v_cvt_pk_bf16_f32 v218, v218, v226
	v_cvt_pk_bf16_f32 v219, v219, v227
	s_mov_b64 exec, s[2:3]
	global_store_dword v[228:229], v212, off nt
	global_store_dword v[228:229], v213, off offset:64 nt
	global_store_dword v[228:229], v214, off offset:128 nt
	global_store_dword v[228:229], v215, off offset:192 nt
	global_store_dword v[228:229], v216, off offset:256 nt
	global_store_dword v[228:229], v217, off offset:320 nt
	global_store_dword v[228:229], v218, off offset:384 nt
	global_store_dword v[228:229], v219, off offset:448 nt
	s_mov_b64 exec, -1
	s_mov_b64 s[60:61], 0x16000
	v_lshl_add_u64 v[228:229], v[146:147], 0, s[60:61]
	v_mul_f32_e32 v230, v121, v141
	v_mul_f32_e32 v231, v105, v141
	v_mul_f32_e32 v232, v89, v141
	v_mul_f32_e32 v233, v73, v141
	v_mul_f32_e32 v234, v57, v141
	v_mul_f32_e32 v235, v41, v141
	v_mul_f32_e32 v236, v25, v141
	v_mul_f32_e32 v237, v9, v141
	v_mov_b32_dpp v238, v230 quad_perm:[1,0,3,2] row_mask:0xf bank_mask:0xf
	v_mov_b32_dpp v239, v231 quad_perm:[1,0,3,2] row_mask:0xf bank_mask:0xf
	v_mov_b32_dpp v240, v232 quad_perm:[1,0,3,2] row_mask:0xf bank_mask:0xf
	v_mov_b32_dpp v241, v233 quad_perm:[1,0,3,2] row_mask:0xf bank_mask:0xf
	v_mov_b32_dpp v242, v234 quad_perm:[1,0,3,2] row_mask:0xf bank_mask:0xf
	v_mov_b32_dpp v243, v235 quad_perm:[1,0,3,2] row_mask:0xf bank_mask:0xf
	v_mov_b32_dpp v244, v236 quad_perm:[1,0,3,2] row_mask:0xf bank_mask:0xf
	v_mov_b32_dpp v245, v237 quad_perm:[1,0,3,2] row_mask:0xf bank_mask:0xf
	v_cvt_pk_bf16_f32 v230, v230, v238
	v_cvt_pk_bf16_f32 v231, v231, v239
	v_cvt_pk_bf16_f32 v232, v232, v240
	v_cvt_pk_bf16_f32 v233, v233, v241
	v_cvt_pk_bf16_f32 v234, v234, v242
	v_cvt_pk_bf16_f32 v235, v235, v243
	v_cvt_pk_bf16_f32 v236, v236, v244
	v_cvt_pk_bf16_f32 v237, v237, v245
	s_mov_b64 exec, s[2:3]
	global_store_dword v[228:229], v230, off nt
	global_store_dword v[228:229], v231, off offset:64 nt
	global_store_dword v[228:229], v232, off offset:128 nt
	global_store_dword v[228:229], v233, off offset:192 nt
	global_store_dword v[228:229], v234, off offset:256 nt
	global_store_dword v[228:229], v235, off offset:320 nt
	global_store_dword v[228:229], v236, off offset:384 nt
	global_store_dword v[228:229], v237, off offset:448 nt
	s_mov_b64 exec, -1
	s_mov_b64 s[60:61], 0x20000
	v_lshl_add_u64 v[228:229], v[146:147], 0, s[60:61]
	v_mul_f32_e32 v212, v122, v134
	v_mul_f32_e32 v213, v106, v134
	v_mul_f32_e32 v214, v90, v134
	v_mul_f32_e32 v215, v74, v134
	v_mul_f32_e32 v216, v58, v134
	v_mul_f32_e32 v217, v42, v134
	v_mul_f32_e32 v218, v26, v134
	v_mul_f32_e32 v219, v10, v134
	v_mov_b32_dpp v220, v212 quad_perm:[1,0,3,2] row_mask:0xf bank_mask:0xf
	v_mov_b32_dpp v221, v213 quad_perm:[1,0,3,2] row_mask:0xf bank_mask:0xf
	v_mov_b32_dpp v222, v214 quad_perm:[1,0,3,2] row_mask:0xf bank_mask:0xf
	v_mov_b32_dpp v223, v215 quad_perm:[1,0,3,2] row_mask:0xf bank_mask:0xf
	v_mov_b32_dpp v224, v216 quad_perm:[1,0,3,2] row_mask:0xf bank_mask:0xf
	v_mov_b32_dpp v225, v217 quad_perm:[1,0,3,2] row_mask:0xf bank_mask:0xf
	v_mov_b32_dpp v226, v218 quad_perm:[1,0,3,2] row_mask:0xf bank_mask:0xf
	v_mov_b32_dpp v227, v219 quad_perm:[1,0,3,2] row_mask:0xf bank_mask:0xf
	v_cvt_pk_bf16_f32 v212, v212, v220
	v_cvt_pk_bf16_f32 v213, v213, v221
	v_cvt_pk_bf16_f32 v214, v214, v222
	v_cvt_pk_bf16_f32 v215, v215, v223
	v_cvt_pk_bf16_f32 v216, v216, v224
	v_cvt_pk_bf16_f32 v217, v217, v225
	v_cvt_pk_bf16_f32 v218, v218, v226
	v_cvt_pk_bf16_f32 v219, v219, v227
	s_mov_b64 exec, s[2:3]
	global_store_dword v[228:229], v212, off nt
	global_store_dword v[228:229], v213, off offset:64 nt
	global_store_dword v[228:229], v214, off offset:128 nt
	global_store_dword v[228:229], v215, off offset:192 nt
	global_store_dword v[228:229], v216, off offset:256 nt
	global_store_dword v[228:229], v217, off offset:320 nt
	global_store_dword v[228:229], v218, off offset:384 nt
	global_store_dword v[228:229], v219, off offset:448 nt
	s_mov_b64 exec, -1
	s_mov_b64 s[60:61], 0x22000
	v_lshl_add_u64 v[228:229], v[146:147], 0, s[60:61]
	v_mul_f32_e32 v230, v123, v135
	v_mul_f32_e32 v231, v107, v135
	v_mul_f32_e32 v232, v91, v135
	v_mul_f32_e32 v233, v75, v135
	v_mul_f32_e32 v234, v59, v135
	v_mul_f32_e32 v235, v43, v135
	v_mul_f32_e32 v236, v27, v135
	v_mul_f32_e32 v237, v11, v135
	v_mov_b32_dpp v238, v230 quad_perm:[1,0,3,2] row_mask:0xf bank_mask:0xf
	v_mov_b32_dpp v239, v231 quad_perm:[1,0,3,2] row_mask:0xf bank_mask:0xf
	v_mov_b32_dpp v240, v232 quad_perm:[1,0,3,2] row_mask:0xf bank_mask:0xf
	v_mov_b32_dpp v241, v233 quad_perm:[1,0,3,2] row_mask:0xf bank_mask:0xf
; __device__ __forceinline__ int crow(int r, int hi) { return (r & 3) + 8 * (r >> 2) + 4 * hi; }
; __device__ __forceinline__ void block(const Blk& B, char* lds, A3_LAS unsigned char* ldsl, const int tid) {
;     ...
;     for (int r = 0; r < 16; ++r) { const int orow = attn::crow(r, hi);
; #pragma unroll
;         for (int d0 = 0; d0 < 8; ++d0) { const float v = o[d0][r] * rli[r]; const float vn = __shfl_xor(v, 1);
;             if ((r32 & 1) == 0) *(unsigned*)(Ow + (size_t)orow * LDO + d0 * 32 + r32) = attn::cvtpk(v, vn); } }
	v_mov_b32_dpp v242, v234 quad_perm:[1,0,3,2] row_mask:0xf bank_mask:0xf
	v_mov_b32_dpp v243, v235 quad_perm:[1,0,3,2] row_mask:0xf bank_mask:0xf
	v_mov_b32_dpp v244, v236 quad_perm:[1,0,3,2] row_mask:0xf bank_mask:0xf
	v_mov_b32_dpp v245, v237 quad_perm:[1,0,3,2] row_mask:0xf bank_mask:0xf
	v_cvt_pk_bf16_f32 v230, v230, v238
	v_cvt_pk_bf16_f32 v231, v231, v239
	v_cvt_pk_bf16_f32 v232, v232, v240
	v_cvt_pk_bf16_f32 v233, v233, v241
	v_cvt_pk_bf16_f32 v234, v234, v242
	v_cvt_pk_bf16_f32 v235, v235, v243
	v_cvt_pk_bf16_f32 v236, v236, v244
	v_cvt_pk_bf16_f32 v237, v237, v245
	s_mov_b64 exec, s[2:3]
	global_store_dword v[228:229], v230, off nt
	global_store_dword v[228:229], v231, off offset:64 nt
	global_store_dword v[228:229], v232, off offset:128 nt
	global_store_dword v[228:229], v233, off offset:192 nt
	global_store_dword v[228:229], v234, off offset:256 nt
	global_store_dword v[228:229], v235, off offset:320 nt
	global_store_dword v[228:229], v236, off offset:384 nt
	global_store_dword v[228:229], v237, off offset:448 nt
	s_mov_b64 exec, -1
	s_mov_b64 s[60:61], 0x24000
	v_lshl_add_u64 v[228:229], v[146:147], 0, s[60:61]
	v_mul_f32_e32 v212, v124, v136
	v_mul_f32_e32 v213, v108, v136
	v_mul_f32_e32 v214, v92, v136
	v_mul_f32_e32 v215, v76, v136
	v_mul_f32_e32 v216, v60, v136
	v_mul_f32_e32 v217, v44, v136
	v_mul_f32_e32 v218, v28, v136
	v_mul_f32_e32 v219, v12, v136
	v_mov_b32_dpp v220, v212 quad_perm:[1,0,3,2] row_mask:0xf bank_mask:0xf
	v_mov_b32_dpp v221, v213 quad_perm:[1,0,3,2] row_mask:0xf bank_mask:0xf
	v_mov_b32_dpp v222, v214 quad_perm:[1,0,3,2] row_mask:0xf bank_mask:0xf
	v_mov_b32_dpp v223, v215 quad_perm:[1,0,3,2] row_mask:0xf bank_mask:0xf
	v_mov_b32_dpp v224, v216 quad_perm:[1,0,3,2] row_mask:0xf bank_mask:0xf
	v_mov_b32_dpp v225, v217 quad_perm:[1,0,3,2] row_mask:0xf bank_mask:0xf
	v_mov_b32_dpp v226, v218 quad_perm:[1,0,3,2] row_mask:0xf bank_mask:0xf
	v_mov_b32_dpp v227, v219 quad_perm:[1,0,3,2] row_mask:0xf bank_mask:0xf
	v_cvt_pk_bf16_f32 v212, v212, v220
	v_cvt_pk_bf16_f32 v213, v213, v221
	v_cvt_pk_bf16_f32 v214, v214, v222
	v_cvt_pk_bf16_f32 v215, v215, v223
	v_cvt_pk_bf16_f32 v216, v216, v224
	v_cvt_pk_bf16_f32 v217, v217, v225
	v_cvt_pk_bf16_f32 v218, v218, v226
	v_cvt_pk_bf16_f32 v219, v219, v227
	s_mov_b64 exec, s[2:3]
	global_store_dword v[228:229], v212, off nt
	global_store_dword v[228:229], v213, off offset:64 nt
	global_store_dword v[228:229], v214, off offset:128 nt
	global_store_dword v[228:229], v215, off offset:192 nt
	global_store_dword v[228:229], v216, off offset:256 nt
	global_store_dword v[228:229], v217, off offset:320 nt
	global_store_dword v[228:229], v218, off offset:384 nt
	global_store_dword v[228:229], v219, off offset:448 nt
	s_mov_b64 exec, -1
	s_mov_b64 s[60:61], 0x26000
	v_lshl_add_u64 v[228:229], v[146:147], 0, s[60:61]
	v_mul_f32_e32 v230, v125, v137
	v_mul_f32_e32 v231, v109, v137
	v_mul_f32_e32 v232, v93, v137
	v_mul_f32_e32 v233, v77, v137
	v_mul_f32_e32 v234, v61, v137
	v_mul_f32_e32 v235, v45, v137
	v_mul_f32_e32 v236, v29, v137
	v_mul_f32_e32 v237, v13, v137
	v_mov_b32_dpp v238, v230 quad_perm:[1,0,3,2] row_mask:0xf bank_mask:0xf
	v_mov_b32_dpp v239, v231 quad_perm:[1,0,3,2] row_mask:0xf bank_mask:0xf
	v_mov_b32_dpp v240, v232 quad_perm:[1,0,3,2] row_mask:0xf bank_mask:0xf
	v_mov_b32_dpp v241, v233 quad_perm:[1,0,3,2] row_mask:0xf bank_mask:0xf
	v_mov_b32_dpp v242, v234 quad_perm:[1,0,3,2] row_mask:0xf bank_mask:0xf
	v_mov_b32_dpp v243, v235 quad_perm:[1,0,3,2] row_mask:0xf bank_mask:0xf
	v_mov_b32_dpp v244, v236 quad_perm:[1,0,3,2] row_mask:0xf bank_mask:0xf
	v_mov_b32_dpp v245, v237 quad_perm:[1,0,3,2] row_mask:0xf bank_mask:0xf
	v_cvt_pk_bf16_f32 v230, v230, v238
	v_cvt_pk_bf16_f32 v231, v231, v239
	v_cvt_pk_bf16_f32 v232, v232, v240
	v_cvt_pk_bf16_f32 v233, v233, v241
	v_cvt_pk_bf16_f32 v234, v234, v242
	v_cvt_pk_bf16_f32 v235, v235, v243
	v_cvt_pk_bf16_f32 v236, v236, v244
	v_cvt_pk_bf16_f32 v237, v237, v245
	s_mov_b64 exec, s[2:3]
	global_store_dword v[228:229], v230, off nt
	global_store_dword v[228:229], v231, off offset:64 nt
	global_store_dword v[228:229], v232, off offset:128 nt
	global_store_dword v[228:229], v233, off offset:192 nt
	global_store_dword v[228:229], v234, off offset:256 nt
	global_store_dword v[228:229], v235, off offset:320 nt
	global_store_dword v[228:229], v236, off offset:384 nt
	global_store_dword v[228:229], v237, off offset:448 nt
	s_mov_b64 exec, -1
	s_mov_b64 s[60:61], 0x30000
	v_lshl_add_u64 v[228:229], v[146:147], 0, s[60:61]
	v_mul_f32_e32 v212, v126, v130
	v_mul_f32_e32 v213, v110, v130
	v_mul_f32_e32 v214, v94, v130
	v_mul_f32_e32 v215, v78, v130
	v_mul_f32_e32 v216, v62, v130
	v_mul_f32_e32 v217, v46, v130
	v_mul_f32_e32 v218, v30, v130
	v_mul_f32_e32 v219, v14, v130
	v_mov_b32_dpp v220, v212 quad_perm:[1,0,3,2] row_mask:0xf bank_mask:0xf
	v_mov_b32_dpp v221, v213 quad_perm:[1,0,3,2] row_mask:0xf bank_mask:0xf
	v_mov_b32_dpp v222, v214 quad_perm:[1,0,3,2] row_mask:0xf bank_mask:0xf
	v_mov_b32_dpp v223, v215 quad_perm:[1,0,3,2] row_mask:0xf bank_mask:0xf
	v_mov_b32_dpp v224, v216 quad_perm:[1,0,3,2] row_mask:0xf bank_mask:0xf
	v_mov_b32_dpp v225, v217 quad_perm:[1,0,3,2] row_mask:0xf bank_mask:0xf
	v_mov_b32_dpp v226, v218 quad_perm:[1,0,3,2] row_mask:0xf bank_mask:0xf
	v_mov_b32_dpp v227, v219 quad_perm:[1,0,3,2] row_mask:0xf bank_mask:0xf
	v_cvt_pk_bf16_f32 v212, v212, v220
	v_cvt_pk_bf16_f32 v213, v213, v221
	v_cvt_pk_bf16_f32 v214, v214, v222
	v_cvt_pk_bf16_f32 v215, v215, v223
	v_cvt_pk_bf16_f32 v216, v216, v224
	v_cvt_pk_bf16_f32 v217, v217, v225
	v_cvt_pk_bf16_f32 v218, v218, v226
	v_cvt_pk_bf16_f32 v219, v219, v227
; __device__ __forceinline__ int crow(int r, int hi) { return (r & 3) + 8 * (r >> 2) + 4 * hi; }
; #define LAS __attribute__((address_space(3)))
; __device__ __forceinline__ int fresh_lane() { int l; asm volatile("v_mbcnt_lo_u32_b32 %0, -1, 0\n\tv_mbcnt_hi_u32_b32 %0, -1, %0" : "=v"(l)); return l; }
; __device__ __forceinline__ KP kargs() { KP kp = (KP)__builtin_amdgcn_kernarg_segment_ptr(); asm volatile("" : "+s"(kp)); return kp; }
; __device__ __forceinline__ void block(const Blk& B, char* lds, A3_LAS unsigned char* ldsl, const int tid) {
;     ...
;     for (int r = 0; r < 16; ++r) { const int orow = attn::crow(r, hi);
; #pragma unroll
;         for (int d0 = 0; d0 < 8; ++d0) { const float v = o[d0][r] * rli[r]; const float vn = __shfl_xor(v, 1);
;             if ((r32 & 1) == 0) *(unsigned*)(Ow + (size_t)orow * LDO + d0 * 32 + r32) = attn::cvtpk(v, vn); } }
;     __syncthreads();
; __device__ __forceinline__ void phase3(KP kp, char* lds, LAS unsigned char* ldsl, int wave, int bid, int G) {
;     ...
; #pragma unroll 1
;         for (int pass = 0; pass < 2; ++pass) {
;             const int qb = (pass ^ ((y ^ j) & 1)) ? y : 31 - y;
;             attn3::Blk B; B.Q = Qb + ((size_t)j * T + (size_t)qb * 256) * 128; B.K = Kb + (size_t)j * T * 128;
;             B.V0 = Vb + (size_t)((j >> 1) * 2) * T * 128; B.V1 = B.V0 + (size_t)T * 128;
;             B.O = OAp + (size_t)(qb * 256) * 4096 + j * 256; B.P0 = qb * 256;
;             const int tid_p = wave * 64 + fresh_lane();
;             attn3::block(B, lds, ldsl, tid_p);
;             if (pass == 0) { conv_run(kargs(), KWS(), (LAS unsigned*)(ldsl + wave * 8320), fresh_lane(), CONV_DENSE_ITEMS + bid * NWAVES + wave, CONV_UP_END, G * NWAVES); __syncthreads(); }
	s_mov_b64 exec, s[2:3]
	global_store_dword v[228:229], v212, off nt
	global_store_dword v[228:229], v213, off offset:64 nt
	global_store_dword v[228:229], v214, off offset:128 nt
	global_store_dword v[228:229], v215, off offset:192 nt
	global_store_dword v[228:229], v216, off offset:256 nt
	global_store_dword v[228:229], v217, off offset:320 nt
	global_store_dword v[228:229], v218, off offset:384 nt
	global_store_dword v[228:229], v219, off offset:448 nt
	s_mov_b64 exec, -1
	s_mov_b64 s[60:61], 0x32000
	v_lshl_add_u64 v[228:229], v[146:147], 0, s[60:61]
	v_mul_f32_e32 v230, v127, v131
	v_mul_f32_e32 v231, v111, v131
	v_mul_f32_e32 v232, v95, v131
	v_mul_f32_e32 v233, v79, v131
	v_mul_f32_e32 v234, v63, v131
	v_mul_f32_e32 v235, v47, v131
	v_mul_f32_e32 v236, v31, v131
	v_mul_f32_e32 v237, v15, v131
	v_mov_b32_dpp v238, v230 quad_perm:[1,0,3,2] row_mask:0xf bank_mask:0xf
	v_mov_b32_dpp v239, v231 quad_perm:[1,0,3,2] row_mask:0xf bank_mask:0xf
	v_mov_b32_dpp v240, v232 quad_perm:[1,0,3,2] row_mask:0xf bank_mask:0xf
	v_mov_b32_dpp v241, v233 quad_perm:[1,0,3,2] row_mask:0xf bank_mask:0xf
	v_mov_b32_dpp v242, v234 quad_perm:[1,0,3,2] row_mask:0xf bank_mask:0xf
	v_mov_b32_dpp v243, v235 quad_perm:[1,0,3,2] row_mask:0xf bank_mask:0xf
	v_mov_b32_dpp v244, v236 quad_perm:[1,0,3,2] row_mask:0xf bank_mask:0xf
	v_mov_b32_dpp v245, v237 quad_perm:[1,0,3,2] row_mask:0xf bank_mask:0xf
	v_cvt_pk_bf16_f32 v230, v230, v238
	v_cvt_pk_bf16_f32 v231, v231, v239
	v_cvt_pk_bf16_f32 v232, v232, v240
	v_cvt_pk_bf16_f32 v233, v233, v241
	v_cvt_pk_bf16_f32 v234, v234, v242
	v_cvt_pk_bf16_f32 v235, v235, v243
	v_cvt_pk_bf16_f32 v236, v236, v244
	v_cvt_pk_bf16_f32 v237, v237, v245
	s_mov_b64 exec, s[2:3]
	global_store_dword v[228:229], v230, off nt
	global_store_dword v[228:229], v231, off offset:64 nt
	global_store_dword v[228:229], v232, off offset:128 nt
	global_store_dword v[228:229], v233, off offset:192 nt
	global_store_dword v[228:229], v234, off offset:256 nt
	global_store_dword v[228:229], v235, off offset:320 nt
	global_store_dword v[228:229], v236, off offset:384 nt
	global_store_dword v[228:229], v237, off offset:448 nt
	s_mov_b64 exec, -1
	s_mov_b64 s[60:61], 0x34000
	v_lshl_add_u64 v[228:229], v[146:147], 0, s[60:61]
	v_mul_f32_e32 v212, v128, v132
	v_mul_f32_e32 v213, v112, v132
	v_mul_f32_e32 v214, v96, v132
	v_mul_f32_e32 v215, v80, v132
	v_mul_f32_e32 v216, v64, v132
	v_mul_f32_e32 v217, v48, v132
	v_mul_f32_e32 v218, v32, v132
	v_mul_f32_e32 v219, v16, v132
	v_mov_b32_dpp v220, v212 quad_perm:[1,0,3,2] row_mask:0xf bank_mask:0xf
	v_mov_b32_dpp v221, v213 quad_perm:[1,0,3,2] row_mask:0xf bank_mask:0xf
	v_mov_b32_dpp v222, v214 quad_perm:[1,0,3,2] row_mask:0xf bank_mask:0xf
	v_mov_b32_dpp v223, v215 quad_perm:[1,0,3,2] row_mask:0xf bank_mask:0xf
	v_mov_b32_dpp v224, v216 quad_perm:[1,0,3,2] row_mask:0xf bank_mask:0xf
	v_mov_b32_dpp v225, v217 quad_perm:[1,0,3,2] row_mask:0xf bank_mask:0xf
	v_mov_b32_dpp v226, v218 quad_perm:[1,0,3,2] row_mask:0xf bank_mask:0xf
	v_mov_b32_dpp v227, v219 quad_perm:[1,0,3,2] row_mask:0xf bank_mask:0xf
	v_cvt_pk_bf16_f32 v212, v212, v220
	v_cvt_pk_bf16_f32 v213, v213, v221
	v_cvt_pk_bf16_f32 v214, v214, v222
	v_cvt_pk_bf16_f32 v215, v215, v223
	v_cvt_pk_bf16_f32 v216, v216, v224
	v_cvt_pk_bf16_f32 v217, v217, v225
	v_cvt_pk_bf16_f32 v218, v218, v226
	v_cvt_pk_bf16_f32 v219, v219, v227
	s_mov_b64 exec, s[2:3]
	global_store_dword v[228:229], v212, off nt
	global_store_dword v[228:229], v213, off offset:64 nt
	global_store_dword v[228:229], v214, off offset:128 nt
	global_store_dword v[228:229], v215, off offset:192 nt
	global_store_dword v[228:229], v216, off offset:256 nt
	global_store_dword v[228:229], v217, off offset:320 nt
	global_store_dword v[228:229], v218, off offset:384 nt
	global_store_dword v[228:229], v219, off offset:448 nt
	s_mov_b64 exec, -1
	s_mov_b64 s[60:61], 0x36000
	v_lshl_add_u64 v[228:229], v[146:147], 0, s[60:61]
	v_mul_f32_e32 v230, v129, v133
	v_mul_f32_e32 v231, v113, v133
	v_mul_f32_e32 v232, v97, v133
	v_mul_f32_e32 v233, v81, v133
	v_mul_f32_e32 v234, v65, v133
	v_mul_f32_e32 v235, v49, v133
	v_mul_f32_e32 v236, v33, v133
	v_mul_f32_e32 v237, v17, v133
	v_mov_b32_dpp v238, v230 quad_perm:[1,0,3,2] row_mask:0xf bank_mask:0xf
	v_mov_b32_dpp v239, v231 quad_perm:[1,0,3,2] row_mask:0xf bank_mask:0xf
	v_mov_b32_dpp v240, v232 quad_perm:[1,0,3,2] row_mask:0xf bank_mask:0xf
	v_mov_b32_dpp v241, v233 quad_perm:[1,0,3,2] row_mask:0xf bank_mask:0xf
	v_mov_b32_dpp v242, v234 quad_perm:[1,0,3,2] row_mask:0xf bank_mask:0xf
	v_mov_b32_dpp v243, v235 quad_perm:[1,0,3,2] row_mask:0xf bank_mask:0xf
	v_mov_b32_dpp v244, v236 quad_perm:[1,0,3,2] row_mask:0xf bank_mask:0xf
	v_mov_b32_dpp v245, v237 quad_perm:[1,0,3,2] row_mask:0xf bank_mask:0xf
	v_cvt_pk_bf16_f32 v230, v230, v238
	v_cvt_pk_bf16_f32 v231, v231, v239
	v_cvt_pk_bf16_f32 v232, v232, v240
	v_cvt_pk_bf16_f32 v233, v233, v241
	v_cvt_pk_bf16_f32 v234, v234, v242
	v_cvt_pk_bf16_f32 v235, v235, v243
	v_cvt_pk_bf16_f32 v236, v236, v244
	v_cvt_pk_bf16_f32 v237, v237, v245
	s_mov_b64 exec, s[2:3]
	global_store_dword v[228:229], v230, off nt
	global_store_dword v[228:229], v231, off offset:64 nt
	global_store_dword v[228:229], v232, off offset:128 nt
	global_store_dword v[228:229], v233, off offset:192 nt
	global_store_dword v[228:229], v234, off offset:256 nt
	global_store_dword v[228:229], v235, off offset:320 nt
	global_store_dword v[228:229], v236, off offset:384 nt
	global_store_dword v[228:229], v237, off offset:448 nt
	s_mov_b64 exec, -1
	s_andn2_b64 vcc, exec, s[54:55]
	s_mov_b64 s[2:3], -1
	s_waitcnt lgkmcnt(0)
	s_barrier
	s_cbranch_vccnz .LBB0_322
	s_mov_b64 s[2:3], s[0:1]
	s_andn2_b64 vcc, exec, s[8:9]
	v_mbcnt_lo_u32_b32 v66, -1, 0
	v_mbcnt_hi_u32_b32 v66, -1, v66
	s_cbranch_vccnz .LBB0_321
	s_mov_b64 s[58:59], -1
	s_and_b64 vcc, exec, s[10:11]
	s_cbranch_vccz .LBB0_611
	s_and_b64 vcc, exec, s[12:13]
	s_cbranch_vccz .LBB0_608
	s_and_b64 vcc, exec, s[14:15]
	s_cbranch_vccz .LBB0_606
	s_mov_b64 s[54:55], -1
	s_and_b64 vcc, exec, s[26:27]
	s_cbranch_vccz .LBB0_603
	s_load_dwordx2 s[4:5], s[2:3], 0x98
	s_mov_b64 s[54:55], 0
	s_waitcnt lgkmcnt(0)
	s_add_u32 s56, s4, s30
	s_addc_u32 s57, s5, s31
